# MoE2: drop the full vmcnt(0) store drain between a unit's epilogue and the next unit (loads are already drained in the epilogue)
# baseline (speedup 1.0000x reference)
; #define PG8_BAR __builtin_amdgcn_s_barrier()
; template <class Epi, class Sched>
; __device__ __forceinline__ void gemm_phase(PG8_LAS unsigned char* lds, const int K, const Sched& S, const Epi& E, const int wave_s) {
;     ...
;         if (wr == 0) PG8_BAR;
;         E(acc, cur, wr, wc, fr, fq);
;         if (!has_next) break;
; #pragma unroll
;         for (int a = 0; a < 2; ++a)
; #pragma unroll
;             for (int b = 0; b < 2; ++b)
; #pragma unroll
;                 for (int m = 0; m < 4; ++m)
; #pragma unroll
;                     for (int n = 0; n < 2; ++n) acc[a][b][m][n] = (f32x4){0.f, 0.f, 0.f, 0.f};
;         cur = nxt; cA = nA; cB = nB; ++ui;
; #pragma unroll
;         for (int h = 0; h < 2; ++h)
; #pragma unroll
;             for (int i = 0; i < 2; ++i) vA[h][i] = vN[h][i];
;         if (wr == 1) PG8_BAR;
.LBB0_1003:
	s_andn2_b64 vcc, exec, s[4:5]
	v_mov_b32_e32 v146, v173
	s_mov_b32 s6, s55
	s_mov_b32 s26, s22
	s_mov_b64 s[10:11], s[30:31]
	s_mov_b64 s[8:9], s[28:29]
	s_cbranch_vccz .LBB0_1040
